# speedup vs baseline: 1.0147x; 1.0147x over previous
_Z10agg_kernelPKDF16_PKiS2_S2_PKfS2_PDF16_Pfi:
	s_load_dwordx8 s[12:19], s[0:1], 0x0
	s_lshl_b32 s4, s2, 1
	s_ashr_i32 s5, s4, 31
	s_lshl_b64 s[4:5], s[4:5], 2
	v_and_b32_e32 v1, 63, v0
	s_waitcnt lgkmcnt(0)
	s_add_u32 s20, s16, s4
	s_addc_u32 s21, s17, s5
	s_load_dwordx2 s[16:17], s[20:21], 0x0
	s_load_dwordx8 s[4:11], s[0:1], 0x20
	v_readfirstlane_b32 s3, v0
	v_lshlrev_b32_e32 v2, 2, v1
	s_lshr_b32 s3, s3, 6
	s_waitcnt lgkmcnt(0)
	s_ashr_i32 s21, s16, 31
	s_mov_b32 s20, s16
	global_load_dword v3, v2, s[6:7]
	global_load_dword v4, v2, s[6:7] offset:256
	global_load_dword v6, v2, s[6:7] offset:512
	global_load_dword v5, v2, s[6:7] offset:768
	s_lshl_b64 s[6:7], s[20:21], 2
	s_add_u32 s6, s14, s6
	s_addc_u32 s7, s15, s7
	s_add_i32 s21, s17, 15
	s_ashr_i32 s21, s21, 4
	s_max_i32 s20, s21, 1
	s_add_i32 s20, s20, -1
	s_min_u32 s14, s3, s20
	s_lshl_b32 s30, s14, 4
	v_mov_b32_e32 v59, 0x30e0000
	v_bfe_u32 v2, v0, 4, 2
	v_lshlrev_b32_e32 v7, 2, v0
	s_lshl_b32 s14, s14, 6
	v_and_or_b32 v18, v7, 12, v2
	s_add_u32 s14, s6, s14
	s_addc_u32 s15, s7, 0
	v_lshlrev_b32_e32 v2, 2, v18
	global_load_dword v2, v2, s[14:15] nt
	v_lshlrev_b32_e32 v20, 2, v18
	v_mov_b32_e32 v8, 0
	v_or_b32_e32 v9, 0xfffffc00, v0
	s_mov_b64 s[14:15], 0
	s_movk_i32 s16, 0x762f
.LBB2_1:
	v_add_u32_e32 v9, 0x400, v9
	v_cmp_lt_u32_e32 vcc, s16, v9
	ds_write_b32 v7, v8
	s_or_b64 s[14:15], vcc, s[14:15]
	v_add_u32_e32 v7, 0x1000, v7
	s_andn2_b64 exec, exec, s[14:15]
	s_cbranch_execnz .LBB2_1
	s_or_b64 exec, exec, s[14:15]
	s_waitcnt vmcnt(2)
	v_max3_i32 v3, v3, v4, v6
	v_mbcnt_lo_u32_b32 v4, -1, 0
	v_mbcnt_hi_u32_b32 v4, -1, v4
	v_and_b32_e32 v25, 64, v4
	s_waitcnt vmcnt(1)
	v_max3_i32 v3, v3, v5, 0
	v_add_u32_e32 v5, 64, v25
	v_xor_b32_e32 v6, 1, v4
	v_cmp_lt_i32_e32 vcc, v6, v5
	s_load_dword s16, s[0:1], 0x40
	s_mul_i32 s14, s2, 0x187
	v_cndmask_b32_e32 v6, v4, v6, vcc
	v_lshlrev_b32_e32 v6, 2, v6
	ds_bpermute_b32 v6, v6, v3
	s_waitcnt lgkmcnt(0)
	s_sub_i32 s15, s16, s14
	s_movk_i32 s0, 0x73
	s_cmp_gt_i32 s21, s3
	s_cselect_b64 s[22:23], -1, 0
	v_max_i32_e32 v3, v3, v6
	v_xor_b32_e32 v6, 2, v4
	v_cmp_lt_i32_e32 vcc, v6, v5
	v_mov_b32_e32 v29, 0
	v_mov_b32_e32 v27, 0
	v_cndmask_b32_e32 v6, v4, v6, vcc
	v_lshlrev_b32_e32 v6, 2, v6
	ds_bpermute_b32 v6, v6, v3
	v_mov_b32_e32 v28, 0
	v_mov_b32_e32 v26, 0
	v_mov_b32_e32 v21, 0
	s_waitcnt vmcnt(0)
	v_add_u32_e32 v33, s30, v18
	v_cmp_gt_i32_e64 s[28:29], s17, v33
	s_nop 1
	v_cndmask_b32_e64 v2, v59, v2, s[28:29]
	s_nop 1
	v_mov_b32_dpp v29, v2 row_newbcast:0 row_mask:0xf bank_mask:0xf
	s_waitcnt lgkmcnt(0)
	v_max_i32_e32 v3, v3, v6
	v_xor_b32_e32 v6, 4, v4
	v_cmp_lt_i32_e32 vcc, v6, v5
	v_mov_b32_dpp v27, v2 row_newbcast:1 row_mask:0xf bank_mask:0xf
	v_mov_b32_dpp v28, v2 row_newbcast:2 row_mask:0xf bank_mask:0xf
	v_cndmask_b32_e32 v6, v4, v6, vcc
	v_lshlrev_b32_e32 v6, 2, v6
	ds_bpermute_b32 v6, v6, v3
	v_mov_b32_dpp v26, v2 row_newbcast:3 row_mask:0xf bank_mask:0xf
	s_waitcnt lgkmcnt(0)
	s_barrier
	v_max_i32_e32 v3, v3, v6
	v_xor_b32_e32 v6, 8, v4
	v_cmp_lt_i32_e32 vcc, v6, v5
	s_nop 1
	v_cndmask_b32_e32 v6, v4, v6, vcc
	v_lshlrev_b32_e32 v60, 2, v6
	ds_bpermute_b32 v6, v60, v3
	s_waitcnt lgkmcnt(0)
	v_max_i32_e32 v3, v3, v6
	v_xor_b32_e32 v6, 16, v4
	v_cmp_lt_i32_e32 vcc, v6, v5
	s_nop 1
	v_cndmask_b32_e32 v6, v4, v6, vcc
	v_lshlrev_b32_e32 v61, 2, v6
	ds_bpermute_b32 v6, v61, v3
	s_waitcnt lgkmcnt(0)
	v_max_i32_e32 v3, v3, v6
	v_xor_b32_e32 v6, 32, v4
	v_cmp_lt_i32_e32 vcc, v6, v5
	v_and_b32_e32 v5, 15, v0
	v_lshlrev_b32_e32 v24, 4, v5
	v_cndmask_b32_e32 v4, v4, v6, vcc
	v_lshlrev_b32_e32 v66, 2, v4
	ds_bpermute_b32 v4, v66, v3
	v_lshlrev_b32_e32 v23, 2, v5
	s_waitcnt lgkmcnt(0)
	v_max_i32_e32 v3, v3, v4
	v_lshrrev_b32_e32 v3, 23, v3
	v_mov_b32_e32 v4, 0x8b
	v_med3_u32 v3, v3, s0, v4
	s_sub_i32 s0, s21, s3
	s_add_i32 s0, s0, 15
	s_cmp_gt_u32 s0, 15
	s_cselect_b64 s[24:25], -1, 0
	v_lshlrev_b32_e32 v19, 23, v3
	s_and_b64 s[22:23], s[22:23], s[24:25]
	v_sub_u32_e32 v22, 0x84800000, v19
	s_and_b64 vcc, exec, s[22:23]
	s_cbranch_vccz .LBB2_5
	s_lshr_b32 s21, s0, 4
	s_mov_b32 s1, 0
	s_mov_b32 s22, 0x1ffff00
	s_mov_b32 s23, 0x4b400000
	v_lshl_add_u64 v[20:21], s[6:7], 0, v[20:21]
	s_add_i32 s0, s3, 16
	s_mov_b32 s24, s0
	s_min_i32 s24, s24, s20
	s_lshl_b32 s24, s24, 4
	s_ashr_i32 s25, s24, 31
	v_lshl_add_u64 v[32:33], s[24:25], 2, v[20:21]
	global_load_dword v30, v[32:33], off nt
	v_lshlrev_b32_e32 v35, 8, v29
	v_and_or_b32 v35, v35, s22, v24
	global_load_dwordx4 v[2:5], v35, s[12:13]
	v_lshlrev_b32_e32 v35, 8, v27
	v_and_or_b32 v35, v35, s22, v24
	global_load_dwordx4 v[6:9], v35, s[12:13]
	v_lshlrev_b32_e32 v35, 8, v28
	v_and_or_b32 v35, v35, s22, v24
	global_load_dwordx4 v[10:13], v35, s[12:13]
	v_lshlrev_b32_e32 v35, 8, v26
	v_and_or_b32 v35, v35, s22, v24
	global_load_dwordx4 v[14:17], v35, s[12:13]
.Lagg_loop:
	s_waitcnt vmcnt(4)
	s_mov_b32 s24, s0
	s_min_i32 s24, s24, s20
	s_lshl_b32 s24, s24, 4
	v_add_u32_e32 v33, s24, v18
	v_cmp_gt_i32_e64 s[28:29], s17, v33
	s_add_i32 s24, s0, 16
	s_min_i32 s24, s24, s20
	s_lshl_b32 s24, s24, 4
	s_ashr_i32 s25, s24, 31
	v_cndmask_b32_e64 v31, v59, v30, s[28:29]
	v_lshl_add_u64 v[32:33], s[24:25], 2, v[20:21]
	global_load_dword v30, v[32:33], off nt
	s_waitcnt vmcnt(4)
	v_ashrrev_i32_e32 v32, 17, v29
	v_mul_i32_i24_e32 v32, 0x140, v32
	v_fma_mix_f32 v33, v2, v22, s23 op_sel_hi:[1,0,0]
	v_fma_mix_f32 v34, v2, v22, s23 op_sel:[1,0,0] op_sel_hi:[1,0,0]
	v_or_b32_e32 v32, v23, v32
	v_lshl_add_u32 v33, v34, 16, v33
	ds_add_u32 v32, v33
	v_fma_mix_f32 v33, v3, v22, s23 op_sel_hi:[1,0,0]
	v_fma_mix_f32 v34, v3, v22, s23 op_sel:[1,0,0] op_sel_hi:[1,0,0]
	s_nop 0
	v_lshl_add_u32 v33, v34, 16, v33
	ds_add_u32 v32, v33 offset:64
	v_fma_mix_f32 v33, v4, v22, s23 op_sel_hi:[1,0,0]
	v_fma_mix_f32 v34, v4, v22, s23 op_sel:[1,0,0] op_sel_hi:[1,0,0]
	s_nop 0
	v_lshl_add_u32 v33, v34, 16, v33
	ds_add_u32 v32, v33 offset:128
	v_fma_mix_f32 v33, v5, v22, s23 op_sel_hi:[1,0,0]
	v_fma_mix_f32 v34, v5, v22, s23 op_sel:[1,0,0] op_sel_hi:[1,0,0]
	s_nop 0
	v_lshl_add_u32 v33, v34, 16, v33
	ds_add_u32 v32, v33 offset:192
	v_mov_b32_e32 v29, 0
	s_nop 1
	v_mov_b32_dpp v29, v31 row_newbcast:0 row_mask:0xf bank_mask:0xf
	v_lshlrev_b32_e32 v35, 8, v29
	v_and_or_b32 v35, v35, s22, v24
	s_waitcnt vmcnt(1)
	global_load_dwordx4 v[2:5], v35, s[12:13]
	s_waitcnt vmcnt(4)
	v_ashrrev_i32_e32 v32, 17, v27
	v_mul_i32_i24_e32 v32, 0x140, v32
	v_fma_mix_f32 v33, v6, v22, s23 op_sel_hi:[1,0,0]
	v_fma_mix_f32 v34, v6, v22, s23 op_sel:[1,0,0] op_sel_hi:[1,0,0]
	v_or_b32_e32 v32, v23, v32
	v_lshl_add_u32 v33, v34, 16, v33
	ds_add_u32 v32, v33
	v_fma_mix_f32 v33, v7, v22, s23 op_sel_hi:[1,0,0]
	v_fma_mix_f32 v34, v7, v22, s23 op_sel:[1,0,0] op_sel_hi:[1,0,0]
	s_nop 0
	v_lshl_add_u32 v33, v34, 16, v33
	ds_add_u32 v32, v33 offset:64
	v_fma_mix_f32 v33, v8, v22, s23 op_sel_hi:[1,0,0]
	v_fma_mix_f32 v34, v8, v22, s23 op_sel:[1,0,0] op_sel_hi:[1,0,0]
	s_nop 0
	v_lshl_add_u32 v33, v34, 16, v33
	ds_add_u32 v32, v33 offset:128
	v_fma_mix_f32 v33, v9, v22, s23 op_sel_hi:[1,0,0]
	v_fma_mix_f32 v34, v9, v22, s23 op_sel:[1,0,0] op_sel_hi:[1,0,0]
	s_nop 0
	v_lshl_add_u32 v33, v34, 16, v33
	ds_add_u32 v32, v33 offset:192
	v_mov_b32_e32 v27, 0
	s_nop 1
	v_mov_b32_dpp v27, v31 row_newbcast:1 row_mask:0xf bank_mask:0xf
	v_lshlrev_b32_e32 v35, 8, v27
	v_and_or_b32 v35, v35, s22, v24
	s_waitcnt vmcnt(1)
	global_load_dwordx4 v[6:9], v35, s[12:13]
	s_waitcnt vmcnt(4)
	v_ashrrev_i32_e32 v32, 17, v28
	v_mul_i32_i24_e32 v32, 0x140, v32
	v_fma_mix_f32 v33, v10, v22, s23 op_sel_hi:[1,0,0]
	v_fma_mix_f32 v34, v10, v22, s23 op_sel:[1,0,0] op_sel_hi:[1,0,0]
	v_or_b32_e32 v32, v23, v32
	v_lshl_add_u32 v33, v34, 16, v33
	ds_add_u32 v32, v33
	v_fma_mix_f32 v33, v11, v22, s23 op_sel_hi:[1,0,0]
	v_fma_mix_f32 v34, v11, v22, s23 op_sel:[1,0,0] op_sel_hi:[1,0,0]
	s_nop 0
	v_lshl_add_u32 v33, v34, 16, v33
	ds_add_u32 v32, v33 offset:64
	v_fma_mix_f32 v33, v12, v22, s23 op_sel_hi:[1,0,0]
	v_fma_mix_f32 v34, v12, v22, s23 op_sel:[1,0,0] op_sel_hi:[1,0,0]
	s_nop 0
	v_lshl_add_u32 v33, v34, 16, v33
	ds_add_u32 v32, v33 offset:128
	v_fma_mix_f32 v33, v13, v22, s23 op_sel_hi:[1,0,0]
	v_fma_mix_f32 v34, v13, v22, s23 op_sel:[1,0,0] op_sel_hi:[1,0,0]
	s_nop 0
	v_lshl_add_u32 v33, v34, 16, v33
	ds_add_u32 v32, v33 offset:192
	v_mov_b32_e32 v28, 0
	s_nop 1
	v_mov_b32_dpp v28, v31 row_newbcast:2 row_mask:0xf bank_mask:0xf
	v_lshlrev_b32_e32 v35, 8, v28
	v_and_or_b32 v35, v35, s22, v24
	s_waitcnt vmcnt(1)
	global_load_dwordx4 v[10:13], v35, s[12:13]
	s_waitcnt vmcnt(4)
	v_ashrrev_i32_e32 v32, 17, v26
	v_mul_i32_i24_e32 v32, 0x140, v32
	v_fma_mix_f32 v33, v14, v22, s23 op_sel_hi:[1,0,0]
	v_fma_mix_f32 v34, v14, v22, s23 op_sel:[1,0,0] op_sel_hi:[1,0,0]
	v_or_b32_e32 v32, v23, v32
	v_lshl_add_u32 v33, v34, 16, v33
	ds_add_u32 v32, v33
	v_fma_mix_f32 v33, v15, v22, s23 op_sel_hi:[1,0,0]
	v_fma_mix_f32 v34, v15, v22, s23 op_sel:[1,0,0] op_sel_hi:[1,0,0]
	s_nop 0
	v_lshl_add_u32 v33, v34, 16, v33
	ds_add_u32 v32, v33 offset:64
	v_fma_mix_f32 v33, v16, v22, s23 op_sel_hi:[1,0,0]
	v_fma_mix_f32 v34, v16, v22, s23 op_sel:[1,0,0] op_sel_hi:[1,0,0]
	s_nop 0
	v_lshl_add_u32 v33, v34, 16, v33
	ds_add_u32 v32, v33 offset:128
	v_fma_mix_f32 v33, v17, v22, s23 op_sel_hi:[1,0,0]
	v_fma_mix_f32 v34, v17, v22, s23 op_sel:[1,0,0] op_sel_hi:[1,0,0]
	s_nop 0
	v_lshl_add_u32 v33, v34, 16, v33
	ds_add_u32 v32, v33 offset:192
	v_mov_b32_e32 v26, 0
	s_nop 1
	v_mov_b32_dpp v26, v31 row_newbcast:3 row_mask:0xf bank_mask:0xf
	v_lshlrev_b32_e32 v35, 8, v26
	v_and_or_b32 v35, v35, s22, v24
	s_waitcnt vmcnt(1)
	global_load_dwordx4 v[14:17], v35, s[12:13]
	s_add_i32 s1, s1, 1
	s_add_i32 s0, s0, 16
	s_cmp_lt_u32 s1, s21
	s_cbranch_scc1 .Lagg_loop
.Lagg_done:
	s_waitcnt vmcnt(0)
.LBB2_5:
	s_min_i32 s15, s15, 0x187
.LBB2_15:
	v_lshrrev_b32_e32 v43, 3, v0
	s_waitcnt vmcnt(0)
	v_add_u32_e32 v2, s14, v43
	s_add_i32 s16, s16, -1
	v_add_u32_e32 v3, 0x80, v2
	v_min_i32_e32 v4, s16, v3
	v_ashrrev_i32_e32 v5, 31, v4
	v_lshlrev_b64 v[6:7], 2, v[4:5]
	v_lshl_add_u64 v[4:5], s[4:5], 0, v[6:7]
	v_lshl_add_u64 v[6:7], s[18:19], 0, v[6:7]
	v_add_u32_e32 v3, 0x100, v2
	global_load_dword v4, v[4:5], off
	v_mov_b32_e32 v38, 0
	global_load_dword v5, v[6:7], off
	v_min_i32_e32 v6, s16, v3
	v_ashrrev_i32_e32 v7, 31, v6
	v_lshlrev_b64 v[6:7], 2, v[6:7]
	v_lshl_add_u64 v[8:9], s[4:5], 0, v[6:7]
	v_lshl_add_u64 v[6:7], s[18:19], 0, v[6:7]
	v_add_u32_e32 v3, 0x180, v2
	global_load_dword v49, v[6:7], off
	v_min_i32_e32 v6, s16, v3
	v_ashrrev_i32_e32 v7, 31, v6
	v_lshlrev_b64 v[6:7], 2, v[6:7]
	global_load_dword v48, v[8:9], off
	v_lshl_add_u64 v[8:9], s[4:5], 0, v[6:7]
	v_lshl_add_u64 v[6:7], s[18:19], 0, v[6:7]
	global_load_dword v44, v[8:9], off
	global_load_dword v46, v[6:7], off
	v_lshlrev_b32_e32 v3, 3, v0
	v_and_b32_e32 v42, 56, v3
	v_add_u32_e32 v45, 0xfa800000, v19
	v_lshlrev_b32_e32 v47, 2, v42
	v_cmp_gt_i32_e32 vcc, s15, v43
	v_mov_b32_e32 v39, 0
	v_mov_b32_e32 v34, 0
	v_mov_b32_e32 v35, v38
	v_mov_b32_e32 v30, v38
	v_mov_b32_e32 v31, v38
	v_mov_b32_e32 v24, v38
	v_mov_b32_e32 v25, v38
	v_mov_b32_e32 v20, v38
	v_mov_b32_e32 v21, v38
	v_mov_b32_e32 v16, v38
	v_mov_b32_e32 v17, v38
	v_mov_b32_e32 v14, v38
	v_mov_b32_e32 v15, v38
	v_mov_b32_e32 v10, v38
	v_mov_b32_e32 v11, v38
	v_mov_b32_e32 v40, 0
	v_mov_b32_e32 v41, 0
	v_mov_b32_e32 v36, 0
	v_mov_b32_e32 v37, v38
	v_mov_b32_e32 v32, v38
	v_mov_b32_e32 v33, v38
	v_mov_b32_e32 v26, v38
	v_mov_b32_e32 v27, v38
	v_mov_b32_e32 v28, v38
	v_mov_b32_e32 v29, v38
	v_mov_b32_e32 v22, v38
	v_mov_b32_e32 v23, v38
	v_mov_b32_e32 v18, v38
	v_mov_b32_e32 v19, v38
	v_mov_b32_e32 v12, v38
	v_mov_b32_e32 v13, v38
	s_waitcnt lgkmcnt(0)
	s_barrier
	s_and_saveexec_b64 s[0:1], vcc
	s_cbranch_execz .LBB2_17
	v_min_i32_e32 v6, s16, v2
	v_ashrrev_i32_e32 v7, 31, v6
	v_lshlrev_b64 v[6:7], 2, v[6:7]
	v_lshl_add_u64 v[8:9], s[4:5], 0, v[6:7]
	v_lshl_add_u64 v[6:7], s[18:19], 0, v[6:7]
	global_load_dword v23, v[6:7], off
	global_load_dword v22, v[8:9], off
	s_movk_i32 s5, 0x140
	v_mad_u32_u24 v10, v43, s5, v47
	ds_read_b128 v[6:9], v10
	ds_read_b128 v[10:13], v10 offset:16
	v_ashrrev_i32_e32 v3, 31, v2
	v_lshlrev_b64 v[2:3], 8, v[2:3]
	v_lshlrev_b32_e32 v14, 1, v42
	v_mov_b32_e32 v15, 0
	v_lshl_add_u64 v[2:3], s[8:9], 0, v[2:3]
	v_lshl_add_u64 v[2:3], v[2:3], 0, v[14:15]
	s_waitcnt lgkmcnt(1)
	v_cvt_f32_i32_sdwa v15, sext(v7) dst_sel:DWORD dst_unused:UNUSED_PAD src0_sel:WORD_0
	v_cvt_f32_i32_sdwa v14, sext(v6) dst_sel:DWORD dst_unused:UNUSED_PAD src0_sel:WORD_0
	v_cvt_f32_i32_sdwa v17, sext(v9) dst_sel:DWORD dst_unused:UNUSED_PAD src0_sel:WORD_0
	v_cvt_f32_i32_sdwa v16, sext(v8) dst_sel:DWORD dst_unused:UNUSED_PAD src0_sel:WORD_0
	s_waitcnt lgkmcnt(0)
	v_cvt_f32_i32_sdwa v19, sext(v11) dst_sel:DWORD dst_unused:UNUSED_PAD src0_sel:WORD_0
	v_cvt_f32_i32_sdwa v18, sext(v10) dst_sel:DWORD dst_unused:UNUSED_PAD src0_sel:WORD_0
	s_mov_b32 s4, 0xb4c00000
	v_cvt_f32_i32_sdwa v21, sext(v13) dst_sel:DWORD dst_unused:UNUSED_PAD src0_sel:WORD_0
	v_cvt_f32_i32_sdwa v20, sext(v12) dst_sel:DWORD dst_unused:UNUSED_PAD src0_sel:WORD_0
	s_waitcnt vmcnt(1)
	v_mul_lo_u32 v26, v23, s4
	s_waitcnt vmcnt(0)
	v_mul_f32_e32 v28, v22, v45
	v_add_u32_e32 v29, v6, v26
	v_add_u32_e32 v34, v7, v26
	v_add_u32_e32 v35, v8, v26
	v_add_u32_e32 v38, v9, v26
	v_add_u32_e32 v39, v10, v26
	v_add_u32_e32 v52, v11, v26
	v_add_u32_e32 v53, v12, v26
	v_add_u32_e32 v54, v13, v26
	v_pk_mul_f32 v[22:23], v[28:29], v[14:15] op_sel_hi:[0,1]
	v_pk_mul_f32 v[24:25], v[28:29], v[16:17] op_sel_hi:[0,1]
	v_pk_mul_f32 v[30:31], v[28:29], v[18:19] op_sel_hi:[0,1]
	v_pk_fma_f32 v[32:33], v[28:29], v[18:19], 0 op_sel_hi:[0,1,0]
	v_pk_fma_f32 v[36:37], v[28:29], v[16:17], 0 op_sel_hi:[0,1,0]
	v_pk_fma_f32 v[40:41], v[28:29], v[14:15], 0 op_sel_hi:[0,1,0]
	v_sub_u32_sdwa v14, v34, sext(v7) dst_sel:DWORD dst_unused:UNUSED_PAD src0_sel:DWORD src1_sel:WORD_0
	v_sub_u32_sdwa v15, v29, sext(v6) dst_sel:DWORD dst_unused:UNUSED_PAD src0_sel:DWORD src1_sel:WORD_0
	v_sub_u32_sdwa v16, v38, sext(v9) dst_sel:DWORD dst_unused:UNUSED_PAD src0_sel:DWORD src1_sel:WORD_0
	v_sub_u32_sdwa v17, v35, sext(v8) dst_sel:DWORD dst_unused:UNUSED_PAD src0_sel:DWORD src1_sel:WORD_0
	v_sub_u32_sdwa v18, v52, sext(v11) dst_sel:DWORD dst_unused:UNUSED_PAD src0_sel:DWORD src1_sel:WORD_0
	v_sub_u32_sdwa v19, v39, sext(v10) dst_sel:DWORD dst_unused:UNUSED_PAD src0_sel:DWORD src1_sel:WORD_0
	v_sub_u32_sdwa v13, v54, sext(v13) dst_sel:DWORD dst_unused:UNUSED_PAD src0_sel:DWORD src1_sel:WORD_0
	v_sub_u32_sdwa v12, v53, sext(v12) dst_sel:DWORD dst_unused:UNUSED_PAD src0_sel:DWORD src1_sel:WORD_0
	v_cvt_f32_i32_sdwa v11, sext(v14) dst_sel:DWORD dst_unused:UNUSED_PAD src0_sel:WORD_1
	v_cvt_f32_i32_sdwa v10, sext(v15) dst_sel:DWORD dst_unused:UNUSED_PAD src0_sel:WORD_1
	v_cvt_f32_i32_sdwa v15, sext(v16) dst_sel:DWORD dst_unused:UNUSED_PAD src0_sel:WORD_1
	v_cvt_f32_i32_sdwa v14, sext(v17) dst_sel:DWORD dst_unused:UNUSED_PAD src0_sel:WORD_1
	v_cvt_f32_i32_sdwa v17, sext(v18) dst_sel:DWORD dst_unused:UNUSED_PAD src0_sel:WORD_1
	v_cvt_f32_i32_sdwa v16, sext(v19) dst_sel:DWORD dst_unused:UNUSED_PAD src0_sel:WORD_1
	v_cvt_f32_i32_sdwa v13, sext(v13) dst_sel:DWORD dst_unused:UNUSED_PAD src0_sel:WORD_1
	v_cvt_f32_i32_sdwa v12, sext(v12) dst_sel:DWORD dst_unused:UNUSED_PAD src0_sel:WORD_1
	v_pk_mul_f32 v[50:51], v[28:29], v[20:21] op_sel_hi:[0,1]
	v_pk_fma_f32 v[26:27], v[28:29], v[20:21], 0 op_sel_hi:[0,1,0]
	v_pk_mul_f32 v[20:21], v[28:29], v[10:11] op_sel_hi:[0,1]
	v_pk_mul_f32 v[54:55], v[28:29], v[14:15] op_sel_hi:[0,1]
	v_pk_mul_f32 v[56:57], v[28:29], v[16:17] op_sel_hi:[0,1]
	v_pk_mul_f32 v[58:59], v[28:29], v[12:13] op_sel_hi:[0,1]
	v_cvt_pk_f16_f32 v6, v22, v23
	v_cvt_pk_f16_f32 v7, v24, v25
	v_cvt_pk_f16_f32 v8, v30, v31
	v_cvt_pk_f16_f32 v9, v50, v51
	v_pk_mul_f32 v[38:39], v[22:23], v[22:23]
	v_pk_mul_f32 v[34:35], v[24:25], v[24:25]
	v_pk_mul_f32 v[30:31], v[30:31], v[30:31]
	v_pk_mul_f32 v[24:25], v[50:51], v[50:51]
	v_pk_fma_f32 v[12:13], v[28:29], v[12:13], 0 op_sel_hi:[0,1,0]
	v_pk_fma_f32 v[18:19], v[28:29], v[16:17], 0 op_sel_hi:[0,1,0]
	v_pk_fma_f32 v[22:23], v[28:29], v[14:15], 0 op_sel_hi:[0,1,0]
	v_pk_fma_f32 v[28:29], v[28:29], v[10:11], 0 op_sel_hi:[0,1,0]
	v_cvt_pk_f16_f32 v50, v20, v21
	v_pk_mul_f32 v[20:21], v[20:21], v[20:21]
	v_pk_mul_f32 v[16:17], v[54:55], v[54:55]
	v_pk_mul_f32 v[14:15], v[56:57], v[56:57]
	v_pk_mul_f32 v[10:11], v[58:59], v[58:59]
	v_cvt_pk_f16_f32 v51, v54, v55
	v_cvt_pk_f16_f32 v52, v56, v57
	v_cvt_pk_f16_f32 v53, v58, v59
	global_store_dwordx4 v[2:3], v[6:9], off
	global_store_dwordx4 v[2:3], v[50:53], off offset:128

_Z9bn_kernelPKDF16_PKfS2_S2_S2_Pfi:
	s_load_dword s8, s[0:1], 0x30
	s_load_dwordx4 s[4:7], s[0:1], 0x0
	s_load_dwordx4 s[12:15], s[0:1], 0x10
	s_load_dwordx2 s[16:17], s[0:1], 0x20
	s_load_dwordx2 s[18:19], s[0:1], 0x28
	s_load_dword s20, s[0:1], 0x38
	s_lshl_b32 s10, s2, 6
	v_lshrrev_b32_e32 v1, 4, v0
	v_or_b32_e32 v34, s10, v1
	s_waitcnt lgkmcnt(0)
	s_add_i32 s9, s8, -1
	v_min_i32_e32 v6, s9, v34
	v_or_b32_e32 v3, 16, v34
	v_lshlrev_b32_e32 v2, 2, v0
	v_ashrrev_i32_e32 v7, 31, v6
	v_min_i32_e32 v8, s9, v3
	v_and_b32_e32 v4, 60, v2
	v_lshlrev_b64 v[6:7], 8, v[6:7]
	v_ashrrev_i32_e32 v9, 31, v8
	v_mov_b32_e32 v37, 0
	v_lshl_add_u64 v[6:7], s[4:5], 0, v[6:7]
	v_lshlrev_b32_e32 v36, 1, v4
	v_lshlrev_b64 v[8:9], 8, v[8:9]
	v_lshl_add_u64 v[6:7], v[6:7], 0, v[36:37]
	v_lshl_add_u64 v[8:9], s[4:5], 0, v[8:9]
	v_or_b32_e32 v3, 32, v34
	v_lshl_add_u64 v[8:9], v[8:9], 0, v[36:37]
	v_and_b32_e32 v63, 0x1fc, v2
	global_load_dword v64, v63, s[12:13]
	global_load_dword v65, v63, s[14:15]
	global_load_dword v63, v63, s[16:17]
	global_load_dwordx2 v[22:23], v[6:7], off nt
	global_load_dwordx2 v[24:25], v[6:7], off offset:128 nt
	global_load_dwordx2 v[18:19], v[8:9], off nt
	global_load_dwordx2 v[20:21], v[8:9], off offset:128 nt
	v_min_i32_e32 v6, s9, v3
	v_or_b32_e32 v3, 48, v34
	v_min_i32_e32 v8, s9, v3
	v_mov_b32_e32 v3, v37
	v_lshl_add_u64 v[10:11], s[6:7], 0, v[2:3]
	global_load_dword v3, v2, s[6:7]
	global_load_dword v5, v2, s[6:7] offset:1024
	global_load_dword v35, v2, s[6:7] offset:2048
	s_movk_i32 s2, 0x1000
	v_add_co_u32_e32 v12, vcc, s2, v10
	s_movk_i32 s2, 0x2000
	s_nop 0
	v_addc_co_u32_e32 v13, vcc, 0, v11, vcc
	v_add_co_u32_e32 v14, vcc, s2, v10
	s_movk_i32 s2, 0x3000
	s_nop 0
	v_addc_co_u32_e32 v15, vcc, 0, v11, vcc
	global_load_dword v38, v[12:13], off offset:1024
	global_load_dword v39, v[12:13], off offset:2048
	global_load_dword v40, v[12:13], off offset:3072
	v_add_co_u32_e32 v12, vcc, s2, v10
	s_movk_i32 s2, 0x4000
	s_nop 0
	v_addc_co_u32_e32 v13, vcc, 0, v11, vcc
	v_add_co_u32_e32 v16, vcc, s2, v10
	s_movk_i32 s2, 0x5000
	s_nop 0
	v_addc_co_u32_e32 v17, vcc, 0, v11, vcc
	global_load_dword v41, v2, s[6:7] offset:3072
	global_load_dword v42, v[14:15], off offset:-4096
	global_load_dword v43, v[14:15], off
	global_load_dword v44, v[14:15], off offset:1024
	global_load_dword v45, v[14:15], off offset:2048
	global_load_dword v46, v[14:15], off offset:3072
	global_load_dword v47, v[16:17], off offset:-4096
	global_load_dword v48, v[16:17], off
	v_add_co_u32_e32 v14, vcc, s2, v10
	s_movk_i32 s2, 0x6000
	s_nop 0
	v_addc_co_u32_e32 v15, vcc, 0, v11, vcc
	v_add_co_u32_e32 v26, vcc, s2, v10
	v_ashrrev_i32_e32 v7, 31, v6
	s_nop 0
	v_addc_co_u32_e32 v27, vcc, 0, v11, vcc
	global_load_dword v49, v[12:13], off offset:1024
	global_load_dword v50, v[12:13], off offset:2048
	global_load_dword v51, v[12:13], off offset:3072
	global_load_dword v52, v[14:15], off offset:1024
	global_load_dword v53, v[14:15], off offset:2048
	global_load_dword v54, v[14:15], off offset:3072
	global_load_dword v55, v[16:17], off offset:1024
	global_load_dword v56, v[16:17], off offset:2048
	global_load_dword v57, v[16:17], off offset:3072
	global_load_dword v58, v[26:27], off offset:-4096
	global_load_dword v59, v[26:27], off
	global_load_dword v60, v[26:27], off offset:1024
	global_load_dword v61, v[26:27], off offset:2048
	global_load_dword v62, v[26:27], off offset:3072
	v_lshlrev_b64 v[6:7], 8, v[6:7]
	v_ashrrev_i32_e32 v9, 31, v8
	s_movk_i32 s2, 0x7000
	v_lshl_add_u64 v[6:7], s[4:5], 0, v[6:7]
	v_add_co_u32_e32 v10, vcc, s2, v10
	v_lshlrev_b64 v[8:9], 8, v[8:9]
	v_lshl_add_u64 v[6:7], v[6:7], 0, v[36:37]
	v_addc_co_u32_e32 v11, vcc, 0, v11, vcc
	v_lshl_add_u64 v[8:9], s[4:5], 0, v[8:9]
	global_load_dword v12, v[10:11], off
	global_load_dword v13, v[10:11], off offset:1024
	global_load_dword v14, v[10:11], off offset:2048
	global_load_dword v15, v[10:11], off offset:3072
	v_lshl_add_u64 v[8:9], v[8:9], 0, v[36:37]
	global_load_dwordx2 v[30:31], v[6:7], off nt
	global_load_dwordx2 v[32:33], v[6:7], off offset:128 nt
	global_load_dwordx2 v[26:27], v[8:9], off nt
	global_load_dwordx2 v[28:29], v[8:9], off offset:128 nt
	s_movk_i32 s2, 0x80
	v_cmp_gt_u32_e32 vcc, s2, v0
	s_waitcnt vmcnt(35)
	v_add_f32_e32 v3, 0, v3
	s_waitcnt vmcnt(34)
	v_add_f32_e32 v3, v3, v5
	s_waitcnt vmcnt(33)
	v_add_f32_e32 v3, v3, v35
	s_waitcnt vmcnt(29)
	v_add_f32_e32 v3, v3, v41
	s_waitcnt vmcnt(28)
	v_add_f32_e32 v3, v3, v42
	v_add_f32_e32 v3, v3, v38
	v_add_f32_e32 v3, v3, v39
	v_add_f32_e32 v3, v3, v40
	s_waitcnt vmcnt(27)
	v_add_f32_e32 v3, v3, v43
	s_waitcnt vmcnt(26)
	v_add_f32_e32 v3, v3, v44
	s_waitcnt vmcnt(25)
	v_add_f32_e32 v3, v3, v45
	s_waitcnt vmcnt(24)
	v_add_f32_e32 v3, v3, v46
	s_waitcnt vmcnt(23)
	v_add_f32_e32 v3, v3, v47
	s_waitcnt vmcnt(21)
	v_add_f32_e32 v3, v3, v49
	s_waitcnt vmcnt(20)
	v_add_f32_e32 v3, v3, v50
	s_waitcnt vmcnt(19)
	v_add_f32_e32 v3, v3, v51
	v_add_f32_e32 v3, v3, v48
	s_waitcnt vmcnt(15)
	v_add_f32_e32 v3, v3, v55
	s_waitcnt vmcnt(14)
	v_add_f32_e32 v3, v3, v56
	s_waitcnt vmcnt(13)
	v_add_f32_e32 v3, v3, v57
	s_waitcnt vmcnt(12)
	v_add_f32_e32 v3, v3, v58
	v_add_f32_e32 v3, v3, v52
	v_add_f32_e32 v3, v3, v53
	v_add_f32_e32 v3, v3, v54
	s_waitcnt vmcnt(11)
	v_add_f32_e32 v3, v3, v59
	s_waitcnt vmcnt(10)
	v_add_f32_e32 v3, v3, v60
	s_waitcnt vmcnt(9)
	v_add_f32_e32 v3, v3, v61
	s_waitcnt vmcnt(8)
	v_add_f32_e32 v3, v3, v62
	s_waitcnt vmcnt(7)
	v_add_f32_e32 v3, v3, v12
	s_waitcnt vmcnt(6)
	v_add_f32_e32 v3, v3, v13
	s_waitcnt vmcnt(5)
	v_add_f32_e32 v3, v3, v14
	s_waitcnt vmcnt(4)
	v_add_f32_e32 v3, v3, v15
	ds_write_b32 v2, v3
	s_waitcnt lgkmcnt(0)
	s_barrier
	s_and_saveexec_b64 s[2:3], vcc
	s_cbranch_execz .LBB3_2
	v_cvt_f32_i32_e32 v8, s8
	s_mov_b32 s11, 0x800000
	v_mov_b32_e32 v3, v64
	v_mov_b32_e32 v5, v65
	v_div_scale_f32 v10, s[6:7], v8, v8, 1.0
	v_rcp_f32_e32 v11, v10
	ds_read2st64_b32 v[14:15], v2 offset1:2
	v_div_scale_f32 v12, vcc, 1.0, v8, 1.0
	v_fma_f32 v13, -v10, v11, 1.0
	v_fmac_f32_e32 v11, v13, v11
	v_mul_f32_e32 v13, v12, v11
	s_waitcnt lgkmcnt(0)
	v_mov_b32_e32 v7, v14
	v_fma_f32 v14, -v10, v13, v12
	v_fmac_f32_e32 v13, v14, v11
	v_fma_f32 v10, -v10, v13, v12
	v_div_fmas_f32 v10, v10, v11, v13
	v_mov_b32_e32 v6, v15
	v_div_fixup_f32 v8, v10, v8, 1.0
	v_mov_b32_e32 v9, v63
	v_pk_mul_f32 v[6:7], v[8:9], v[6:7] op_sel_hi:[0,1]
	v_fma_f32 v6, -v7, v7, v6
	v_max_f32_e32 v6, 0, v6
	v_add_f32_e32 v6, 0x3727c5ac, v6
	v_mul_f32_e32 v8, 0x4b800000, v6
	v_cmp_gt_f32_e32 vcc, s11, v6
	v_add_f32_e32 v7, v7, v3
	v_sub_f32_e32 v3, v3, v7
	v_cndmask_b32_e32 v6, v6, v8, vcc
	v_rsq_f32_e32 v6, v6
	s_nop 0
	v_mul_f32_e32 v8, 0x45800000, v6
	v_cndmask_b32_e32 v6, v6, v8, vcc
	v_mul_f32_e32 v5, v5, v6
	v_fmac_f32_e32 v9, v3, v5
	ds_write2st64_b32 v2, v5, v9 offset0:4 offset1:6
.LBB3_2:
	s_or_b64 exec, exec, s[2:3]
	v_cmp_gt_i32_e32 vcc, s8, v34
	s_waitcnt lgkmcnt(0)
	s_barrier
	s_and_saveexec_b64 s[2:3], vcc
	s_cbranch_execz .LBB3_11
	v_lshlrev_b32_e32 v40, 2, v4
	s_mov_b64 s[2:3], s[18:19]
	s_mov_b32 s6, s20
	ds_read_b128 v[2:5], v40 offset:1024
	ds_read_b128 v[6:9], v40 offset:1280
	ds_read_b128 v[10:13], v40 offset:1536
	ds_read_b128 v[14:17], v40 offset:1792
	v_ashrrev_i32_e32 v35, 31, v34
	v_mov_b32_e32 v37, 0
	v_lshlrev_b64 v[34:35], 9, v[34:35]
	v_and_b32_e32 v0, 15, v0
	s_waitcnt lgkmcnt(0)
	s_lshl_b32 s0, s6, 6
	v_mov_b32_e32 v41, v37
	v_lshl_or_b32 v34, v0, 4, v34
	v_lshl_add_u64 v[38:39], s[4:5], 0, v[36:37]
	v_lshl_add_u64 v[36:37], s[2:3], 0, v[40:41]
	v_add3_u32 v40, v1, s10, 48
	v_lshl_add_u64 v[0:1], s[2:3], 0, v[34:35]
	s_mov_b64 s[2:3], 0x100
	s_ashr_i32 s1, s0, 31
	v_lshl_add_u64 v[0:1], v[0:1], 0, s[2:3]
	s_lshl_b64 s[2:3], s[0:1], 9
	s_mov_b64 s[4:5], 0
	s_branch .LBB3_5

	.amdhsa_kernel _Z9bn_kernelPKDF16_PKfS2_S2_S2_Pfi
		.amdhsa_group_segment_fixed_size 2048
		.amdhsa_private_segment_fixed_size 0
		.amdhsa_kernarg_size 312
		.amdhsa_user_sgpr_count 2
		.amdhsa_user_sgpr_dispatch_ptr 0
		.amdhsa_user_sgpr_queue_ptr 0
		.amdhsa_user_sgpr_kernarg_segment_ptr 1
		.amdhsa_user_sgpr_dispatch_id 0
		.amdhsa_user_sgpr_kernarg_preload_length 0
		.amdhsa_user_sgpr_kernarg_preload_offset 0
		.amdhsa_user_sgpr_private_segment_size 0
		.amdhsa_uses_dynamic_stack 0
		.amdhsa_enable_private_segment 0
		.amdhsa_system_sgpr_workgroup_id_x 1
		.amdhsa_system_sgpr_workgroup_id_y 0
		.amdhsa_system_sgpr_workgroup_id_z 0
		.amdhsa_system_sgpr_workgroup_info 0
		.amdhsa_system_vgpr_workitem_id 0
		.amdhsa_next_free_vgpr 66
		.amdhsa_next_free_sgpr 21
		.amdhsa_accum_offset 68
		.amdhsa_reserve_vcc 1
		.amdhsa_float_round_mode_32 0
		.amdhsa_float_round_mode_16_64 0
		.amdhsa_float_denorm_mode_32 3
		.amdhsa_float_denorm_mode_16_64 3
		.amdhsa_dx10_clamp 1
		.amdhsa_ieee_mode 1
		.amdhsa_fp16_overflow 0
		.amdhsa_tg_split 0
		.amdhsa_exception_fp_ieee_invalid_op 0
		.amdhsa_exception_fp_denorm_src 0
		.amdhsa_exception_fp_ieee_div_zero 0
		.amdhsa_exception_fp_ieee_overflow 0
		.amdhsa_exception_fp_ieee_underflow 0
		.amdhsa_exception_fp_ieee_inexact 0
		.amdhsa_exception_int_div_zero 0
	.end_amdhsa_kernel
